# ef/d streaming loads use sc0 sc1 nt policy instead of nt
# speedup vs baseline: 1.0089x; 1.0089x over previous
_Z9edge_mainPKfS0_PKiS2_PKcPcS0_S0_Pf:
	s_load_dwordx8 s[8:15], s[0:1], 0x0
	v_and_b32_e32 v2, 16, v0
	v_lshrrev_b32_e32 v1, 6, v0
	v_cmp_eq_u32_e32 vcc, 0, v2
	v_and_b32_e32 v106, 15, v0
	s_waitcnt lgkmcnt(0)
	v_mov_b32_e32 v3, s15
	v_mov_b32_e32 v4, s13
	v_cndmask_b32_e32 v95, v3, v4, vcc
	v_mov_b32_e32 v2, s14
	v_mov_b32_e32 v3, s12
	v_lshl_add_u32 v62, v1, 8, s2
	v_cndmask_b32_e32 v94, v2, v3, vcc
	v_lshl_or_b32 v2, v62, 4, v106
	v_ashrrev_i32_e32 v3, 31, v2
	v_lshl_add_u64 v[4:5], v[2:3], 2, v[94:95]
	v_add_u32_e32 v2, 0x8000, v2
	v_ashrrev_i32_e32 v3, 31, v2
	v_lshl_add_u64 v[2:3], v[2:3], 2, v[94:95]
	global_load_dword v60, v[4:5], off
	global_load_dword v64, v[2:3], off
	s_load_dwordx4 s[12:15], s[0:1], 0x20
	v_and_b32_e32 v70, 63, v0
	v_lshlrev_b32_e32 v68, 4, v70
	v_mov_b32_e32 v69, 0
	v_mov_b32_e32 v2, 0x30d40
	v_bfe_u32 v65, v0, 3, 3
	v_and_b32_e32 v66, 0x70, v68
	v_cndmask_b32_e64 v2, v2, 0, vcc
	v_mov_b32_e32 v3, v69
	v_mov_b32_e32 v67, v69
	s_waitcnt vmcnt(1)
	v_ashrrev_i32_e32 v61, 31, v60
	v_lshlrev_b32_e32 v58, 4, v0
	v_mov_b32_e32 v59, v69
	s_waitcnt lgkmcnt(0)
	v_lshl_add_u64 v[4:5], s[12:13], 0, v[58:59]
	s_movk_i32 s3, 0x2000
	v_add_co_u32_e32 v6, vcc, s3, v4
	s_movk_i32 s3, 0x6000
	s_nop 0
	v_addc_co_u32_e32 v7, vcc, 0, v5, vcc
	global_load_dwordx4 v[72:75], v58, s[12:13]
	v_or_b32_e32 v8, 0x4000, v58
	global_load_dwordx4 v[76:79], v[6:7], off
	global_load_dwordx4 v[80:83], v8, s[12:13]
	v_add_co_u32_e32 v6, vcc, s3, v4
	s_mov_b32 s3, 0xa000
	s_nop 0
	v_addc_co_u32_e32 v7, vcc, 0, v5, vcc
	v_or_b32_e32 v8, 0x8000, v58
	global_load_dwordx4 v[84:87], v[6:7], off
	global_load_dwordx4 v[88:91], v8, s[12:13]
	v_add_co_u32_e32 v6, vcc, s3, v4
	s_mov_b32 s3, 0xe000
	s_nop 0
	v_addc_co_u32_e32 v7, vcc, 0, v5, vcc
	v_lshl_add_u64 v[2:3], s[12:13], 0, v[2:3]
	s_mov_b64 s[4:5], 0x100000
	v_ashrrev_i32_e32 v63, 31, v62
	v_add_co_u32_e32 v4, vcc, s3, v4
	v_lshl_add_u64 v[96:97], v[2:3], 0, s[4:5]
	v_lshlrev_b64 v[2:3], 13, v[62:63]
	v_addc_co_u32_e32 v5, vcc, 0, v5, vcc
	v_lshl_add_u64 v[2:3], s[8:9], 0, v[2:3]
	v_or_b32_e32 v8, 0xc000, v58
	global_load_dwordx4 v[102:105], v[6:7], off
	global_load_dwordx4 v[110:113], v8, s[12:13]
	s_movk_i32 s3, 0x1000
	v_or_b32_e32 v6, 0x1200, v0
	v_cmp_gt_u32_e32 vcc, 32, v0
	v_lshl_add_u64 v[18:19], v[2:3], 0, v[68:69]
	v_add_co_u32_e64 v34, s[4:5], s3, v18
	v_cndmask_b32_e32 v6, 0, v6, vcc
	v_lshlrev_b32_e32 v6, 4, v6
	v_addc_co_u32_e64 v35, s[4:5], 0, v19, s[4:5]
	v_mbcnt_lo_u32_b32 v36, -1, 0
	global_load_dwordx4 v[114:117], v[4:5], off
	global_load_dwordx4 v[54:57], v6, s[12:13]
	s_nop 0
	global_load_dwordx4 v[2:5], v[18:19], off sc0 sc1 nt
	global_load_dwordx4 v[6:9], v[18:19], off offset:1024 sc0 sc1 nt
	global_load_dwordx4 v[10:13], v[18:19], off offset:2048 sc0 sc1 nt
	global_load_dwordx4 v[14:17], v[18:19], off offset:3072 sc0 sc1 nt
	s_nop 0
	global_load_dwordx4 v[18:21], v[34:35], off sc0 sc1 nt
	global_load_dwordx4 v[22:25], v[34:35], off offset:1024 sc0 sc1 nt
	global_load_dwordx4 v[26:29], v[34:35], off offset:2048 sc0 sc1 nt
	global_load_dwordx4 v[30:33], v[34:35], off offset:3072 sc0 sc1 nt
	v_lshlrev_b64 v[34:35], 10, v[62:63]
	v_mbcnt_hi_u32_b32 v63, -1, v36
	v_and_or_b32 v36, v63, 64, v65
	v_lshlrev_b32_e32 v107, 2, v36
	ds_bpermute_b32 v38, v107, v60
	ds_bpermute_b32 v40, v107, v60 offset:32
	v_lshl_add_u64 v[46:47], s[12:13], 0, v[66:67]
	s_mov_b64 s[4:5], 0x200000
	v_lshl_add_u64 v[98:99], v[46:47], 0, s[4:5]
	v_lshl_add_u64 v[34:35], s[10:11], 0, v[34:35]
	s_waitcnt lgkmcnt(1)
	v_lshlrev_b32_e32 v38, 7, v38
	v_mov_b32_e32 v39, v69
	v_lshl_add_u64 v[34:35], v[34:35], 0, v[68:69]
	v_lshl_add_u64 v[48:49], v[98:99], 0, v[38:39]
	s_waitcnt lgkmcnt(0)
	v_lshlrev_b32_e32 v38, 7, v40
	global_load_dwordx4 v[34:37], v[34:35], off sc0 sc1 nt
	v_lshl_add_u64 v[50:51], v[98:99], 0, v[38:39]
	global_load_dwordx4 v[38:41], v[48:49], off
	global_load_dwordx4 v[42:45], v[50:51], off
	ds_bpermute_b32 v48, v107, v60 offset:64
	ds_bpermute_b32 v49, v107, v60 offset:96
	s_mov_b64 s[4:5], 0x81a800
	v_lshl_add_u64 v[100:101], v[46:47], 0, s[4:5]
	v_mov_b32_e32 v47, v69
	s_waitcnt lgkmcnt(1)
	v_lshlrev_b32_e32 v46, 7, v48
	v_lshl_add_u64 v[92:93], v[100:101], 0, v[46:47]
	s_waitcnt lgkmcnt(0)
	v_lshlrev_b32_e32 v46, 7, v49
	v_lshl_add_u64 v[108:109], v[100:101], 0, v[46:47]
	v_lshl_add_u64 v[60:61], v[60:61], 2, v[96:97]
	global_load_dwordx4 v[46:49], v[92:93], off
	global_load_dwordx4 v[50:53], v[108:109], off
	v_or_b32_e32 v59, 0x1000, v0
	global_load_dword v108, v[60:61], off
	v_lshl_or_b32 v60, s2, 3, v1
	v_mov_b32_e32 v61, v69
	v_lshlrev_b64 v[60:61], 11, v[60:61]
	s_movk_i32 s3, 0x1220
	v_lshl_add_u64 v[60:61], s[14:15], 0, v[60:61]
	v_lshlrev_b32_e32 v92, 2, v70
	v_mov_b32_e32 v93, v69
	v_cmp_gt_u32_e64 s[4:5], s3, v59
	v_lshl_add_u64 v[60:61], v[60:61], 0, v[92:93]
	s_mov_b64 s[6:7], 0x2000000
	s_brev_b32 s3, 64
	v_lshl_add_u64 v[92:93], v[60:61], 0, s[6:7]
	v_add_co_u32_e64 v60, s[6:7], s3, v60
	s_nop 1
	v_addc_co_u32_e64 v61, s[6:7], 0, v61, s[6:7]
	global_store_dword v[60:61], v69, off
	global_store_dword v[92:93], v69, off offset:256
	global_store_dword v[92:93], v69, off offset:512
	global_store_dword v[92:93], v69, off offset:768
	global_store_dword v[92:93], v69, off offset:1024
	global_store_dword v[92:93], v69, off offset:1280
	global_store_dword v[92:93], v69, off offset:1536
	global_store_dword v[92:93], v69, off offset:1792
	s_waitcnt vmcnt(30)
	ds_write_b128 v58, v[72:75]
	s_waitcnt vmcnt(29)
	ds_write_b128 v58, v[76:79] offset:8192
	s_waitcnt vmcnt(28)
	ds_write_b128 v58, v[80:83] offset:16384
	s_waitcnt vmcnt(27)
	ds_write_b128 v58, v[84:87] offset:24576
	s_waitcnt vmcnt(26)
	ds_write_b128 v58, v[88:91] offset:32768
	s_waitcnt vmcnt(25)
	ds_write_b128 v58, v[102:105] offset:40960
	s_waitcnt vmcnt(24)
	ds_write_b128 v58, v[110:113] offset:49152
	s_waitcnt vmcnt(23)
	ds_write_b128 v58, v[114:117] offset:57344
	s_and_saveexec_b64 s[6:7], s[4:5]
	s_cbranch_execz .LBB1_2
	v_cndmask_b32_e64 v60, 0, v59, s[4:5]
	v_mov_b32_e32 v61, v69
	v_lshl_add_u64 v[60:61], v[60:61], 4, s[12:13]
	global_load_dwordx4 v[72:75], v[60:61], off
	v_lshlrev_b32_e32 v59, 4, v59
	s_waitcnt vmcnt(0)
	ds_write_b128 v59, v[72:75]

.LBB1_6:
	s_waitcnt vmcnt(14)
	ds_write_b128 v119, v[38:41]
	s_waitcnt vmcnt(13)
	ds_write_b128 v119, v[42:45] offset:2304
	s_waitcnt vmcnt(12)
	ds_write_b128 v119, v[46:49] offset:4608
	s_waitcnt vmcnt(11)
	ds_write_b128 v119, v[50:53] offset:6912
	ds_bpermute_b32 v42, v107, v64
	ds_bpermute_b32 v43, v109, v64
	ds_bpermute_b32 v44, v110, v64
	v_add_u32_e32 v0, 0x1000, v62
	ds_bpermute_b32 v50, v111, v64
	v_min_i32_e32 v0, 0x927b, v0
	v_lshl_or_b32 v40, v0, 4, v106
	s_waitcnt lgkmcnt(3)
	v_lshlrev_b32_e32 v0, 7, v42
	v_ashrrev_i32_e32 v65, 31, v64
	v_lshl_add_u64 v[46:47], v[98:99], 0, v[0:1]
	s_waitcnt lgkmcnt(2)
	v_lshlrev_b32_e32 v0, 7, v43
	v_lshl_add_u64 v[38:39], v[64:65], 2, v[96:97]
	v_ashrrev_i32_e32 v41, 31, v40
	v_lshl_add_u64 v[48:49], v[98:99], 0, v[0:1]
	s_waitcnt lgkmcnt(1)
	v_lshlrev_b32_e32 v0, 7, v44
	s_waitcnt vmcnt(10)
	ds_bpermute_b32 v68, v114, v108
	ds_bpermute_b32 v66, v115, v108
	global_load_dword v108, v[38:39], off
	v_lshl_add_u64 v[38:39], v[40:41], 2, v[94:95]
	v_lshl_add_u64 v[64:65], v[100:101], 0, v[0:1]
	s_waitcnt lgkmcnt(2)
	v_lshlrev_b32_e32 v0, 7, v50
	global_load_dword v135, v[38:39], off
	s_nop 0
	global_load_dwordx4 v[38:41], v[46:47], off
	global_load_dwordx4 v[42:45], v[48:49], off
	v_lshl_add_u64 v[70:71], v[100:101], 0, v[0:1]
	global_load_dwordx4 v[46:49], v[64:65], off
	global_load_dwordx4 v[50:53], v[70:71], off
	ds_read_b128 v[70:73], v120
	ds_read_b128 v[74:77], v120 offset:64
	ds_read_b128 v[78:81], v120 offset:4608
	ds_read_b128 v[82:85], v120 offset:4672
	v_add_u32_e32 v0, 0x800, v62
	ds_write_b128 v121, v[2:5]
	ds_write_b128 v121, v[6:9] offset:1088
	ds_write_b128 v121, v[10:13] offset:2176
	ds_write_b128 v121, v[14:17] offset:3264
	ds_write_b128 v121, v[18:21] offset:4352
	ds_write_b128 v121, v[22:25] offset:5440
	s_waitcnt vmcnt(15)
	ds_write_b128 v121, v[26:29] offset:6528
	s_waitcnt vmcnt(14)
	ds_write_b128 v121, v[30:33] offset:7616
	ds_write_b128 v122, v[34:37] offset:8704
	v_min_i32_e32 v2, 0x927b, v0
	v_ashrrev_i32_e32 v3, 31, v2
	v_lshlrev_b64 v[4:5], 13, v[2:3]
	v_lshlrev_b64 v[2:3], 10, v[2:3]
	v_lshl_add_u64 v[18:19], v[102:103], 0, v[4:5]
	v_lshl_add_u64 v[62:63], v[104:105], 0, v[2:3]
	v_add_co_u32_e32 v64, vcc, s3, v18
	global_load_dwordx4 v[2:5], v[18:19], off sc0 sc1 nt
	global_load_dwordx4 v[6:9], v[18:19], off offset:1024 sc0 sc1 nt
	global_load_dwordx4 v[10:13], v[18:19], off offset:2048 sc0 sc1 nt
	global_load_dwordx4 v[14:17], v[18:19], off offset:3072 sc0 sc1 nt
	v_addc_co_u32_e32 v65, vcc, 0, v19, vcc
	global_load_dwordx4 v[34:37], v[62:63], off sc0 sc1 nt
	global_load_dwordx4 v[18:21], v[64:65], off sc0 sc1 nt
	global_load_dwordx4 v[22:25], v[64:65], off offset:1024 sc0 sc1 nt
	global_load_dwordx4 v[26:29], v[64:65], off offset:2048 sc0 sc1 nt
	global_load_dwordx4 v[30:33], v[64:65], off offset:3072 sc0 sc1 nt
	s_waitcnt lgkmcnt(13)
	v_add_f32_e32 v67, v68, v66
	v_mul_f32_e32 v184, 0xc3000000, v67
	s_waitcnt lgkmcnt(12)
	v_cvt_f32_ubyte3_e32 v169, v70
	v_cvt_f32_ubyte2_e32 v168, v70
	v_cvt_f32_ubyte1_e32 v171, v70
	v_cvt_f32_ubyte0_e32 v170, v70
	ds_read_b128 v[62:65], v123
	ds_read_b128 v[86:89], v123 offset:64
	ds_read_b128 v[90:93], v112
	ds_read_b128 v[136:139], v112 offset:4608
	ds_read_b128 v[140:143], v112 offset:9216
	ds_read_b128 v[144:147], v112 offset:13824
	ds_read_b128 v[148:151], v112 offset:18432
	ds_read_b128 v[152:155], v112 offset:23040
	ds_read_b128 v[156:159], v112 offset:27648
	ds_read_b128 v[160:163], v112 offset:32256
	s_waitcnt lgkmcnt(14)
	v_cvt_f32_ubyte1_e32 v165, v78
	v_cvt_f32_ubyte0_e32 v164, v78
	v_cvt_f32_ubyte3_e32 v167, v78
	v_cvt_f32_ubyte2_e32 v166, v78
	v_pk_fma_f32 v[170:171], v[170:171], v[68:69], v[184:185] op_sel_hi:[1,0,0]
	v_pk_fma_f32 v[168:169], v[168:169], v[68:69], v[184:185] op_sel_hi:[1,0,0]
	v_pk_fma_f32 v[164:165], v[164:165], v[66:67], v[170:171] op_sel_hi:[1,0,1]
	v_pk_fma_f32 v[166:167], v[166:167], v[66:67], v[168:169] op_sel_hi:[1,0,1]
	v_cvt_f32_ubyte1_e32 v169, v79
	v_cvt_f32_ubyte0_e32 v168, v79
	v_cvt_f32_ubyte3_e32 v171, v79
	v_cvt_f32_ubyte2_e32 v170, v79
	v_cvt_f32_ubyte3_e32 v79, v71
	v_cvt_f32_ubyte2_e32 v78, v71
	v_cvt_f32_ubyte1_e32 v173, v71
	v_cvt_f32_ubyte0_e32 v172, v71
	v_pk_fma_f32 v[70:71], v[172:173], v[68:69], v[184:185] op_sel_hi:[1,0,0]
	v_pk_fma_f32 v[78:79], v[78:79], v[68:69], v[184:185] op_sel_hi:[1,0,0]
	v_cvt_f32_ubyte3_e32 v173, v72
	v_cvt_f32_ubyte2_e32 v172, v72
	v_cvt_f32_ubyte1_e32 v175, v72
	v_cvt_f32_ubyte0_e32 v174, v72
	v_pk_fma_f32 v[170:171], v[170:171], v[66:67], v[78:79] op_sel_hi:[1,0,1]
	v_pk_fma_f32 v[168:169], v[168:169], v[66:67], v[70:71] op_sel_hi:[1,0,1]
	v_cvt_f32_ubyte1_e32 v71, v80
	v_cvt_f32_ubyte0_e32 v70, v80
	v_cvt_f32_ubyte3_e32 v79, v80
	v_cvt_f32_ubyte2_e32 v78, v80
	v_pk_fma_f32 v[176:177], v[174:175], v[68:69], v[184:185] op_sel_hi:[1,0,0]
	v_pk_fma_f32 v[172:173], v[172:173], v[68:69], v[184:185] op_sel_hi:[1,0,0]
	v_cvt_f32_ubyte2_e32 v80, v73
	v_pk_fma_f32 v[174:175], v[78:79], v[66:67], v[172:173] op_sel_hi:[1,0,1]
	v_pk_fma_f32 v[172:173], v[70:71], v[66:67], v[176:177] op_sel_hi:[1,0,1]
	v_cvt_f32_ubyte1_e32 v177, v73
	v_cvt_f32_ubyte0_e32 v176, v73
	v_cvt_f32_ubyte1_e32 v71, v81
	v_cvt_f32_ubyte0_e32 v70, v81
	v_cvt_f32_ubyte3_e32 v79, v81
	v_cvt_f32_ubyte2_e32 v78, v81
	v_cvt_f32_ubyte3_e32 v81, v73
	v_pk_fma_f32 v[176:177], v[176:177], v[68:69], v[184:185] op_sel_hi:[1,0,0]
	v_pk_fma_f32 v[72:73], v[80:81], v[68:69], v[184:185] op_sel_hi:[1,0,0]
	v_pk_fma_f32 v[70:71], v[70:71], v[66:67], v[176:177] op_sel_hi:[1,0,1]
	v_cvt_f32_ubyte3_e32 v177, v74
	v_cvt_f32_ubyte2_e32 v176, v74
	v_cvt_f32_ubyte1_e32 v179, v74
	v_cvt_f32_ubyte0_e32 v178, v74
	v_pk_fma_f32 v[72:73], v[78:79], v[66:67], v[72:73] op_sel_hi:[1,0,1]
	v_cvt_f32_ubyte1_e32 v79, v82
	v_cvt_f32_ubyte0_e32 v78, v82
	v_cvt_f32_ubyte3_e32 v81, v82
	v_cvt_f32_ubyte2_e32 v80, v82
	v_pk_fma_f32 v[178:179], v[178:179], v[68:69], v[184:185] op_sel_hi:[1,0,0]
	v_pk_fma_f32 v[176:177], v[176:177], v[68:69], v[184:185] op_sel_hi:[1,0,0]
	v_pk_fma_f32 v[78:79], v[78:79], v[66:67], v[178:179] op_sel_hi:[1,0,1]
	v_pk_fma_f32 v[80:81], v[80:81], v[66:67], v[176:177] op_sel_hi:[1,0,1]
	v_cvt_f32_ubyte1_e32 v177, v83
	v_cvt_f32_ubyte0_e32 v176, v83
	v_cvt_f32_ubyte3_e32 v179, v83
	v_cvt_f32_ubyte2_e32 v178, v83
	v_cvt_f32_ubyte3_e32 v83, v75
	v_cvt_f32_ubyte2_e32 v82, v75
	v_cvt_f32_ubyte1_e32 v181, v75
	v_cvt_f32_ubyte0_e32 v180, v75
	v_pk_fma_f32 v[74:75], v[180:181], v[68:69], v[184:185] op_sel_hi:[1,0,0]
	v_pk_fma_f32 v[82:83], v[82:83], v[68:69], v[184:185] op_sel_hi:[1,0,0]
	v_cvt_f32_ubyte3_e32 v181, v76
	v_cvt_f32_ubyte2_e32 v180, v76
	v_cvt_f32_ubyte1_e32 v183, v76
	v_cvt_f32_ubyte0_e32 v182, v76
	v_pk_fma_f32 v[178:179], v[178:179], v[66:67], v[82:83] op_sel_hi:[1,0,1]
	v_pk_fma_f32 v[176:177], v[176:177], v[66:67], v[74:75] op_sel_hi:[1,0,1]
	v_cvt_f32_ubyte1_e32 v75, v84
	v_cvt_f32_ubyte0_e32 v74, v84
	v_cvt_f32_ubyte3_e32 v83, v84
	v_cvt_f32_ubyte2_e32 v82, v84
	v_pk_fma_f32 v[186:187], v[182:183], v[68:69], v[184:185] op_sel_hi:[1,0,0]
	v_pk_fma_f32 v[180:181], v[180:181], v[68:69], v[184:185] op_sel_hi:[1,0,0]
	v_cvt_f32_ubyte2_e32 v84, v77
	v_pk_fma_f32 v[182:183], v[82:83], v[66:67], v[180:181] op_sel_hi:[1,0,1]
	v_pk_fma_f32 v[180:181], v[74:75], v[66:67], v[186:187] op_sel_hi:[1,0,1]
	v_cvt_f32_ubyte1_e32 v75, v85
	v_cvt_f32_ubyte0_e32 v74, v85
	v_cvt_f32_ubyte3_e32 v83, v85
	v_cvt_f32_ubyte2_e32 v82, v85
	v_cvt_f32_ubyte3_e32 v85, v77
	v_cvt_f32_ubyte1_e32 v187, v77
	v_cvt_f32_ubyte0_e32 v186, v77
	v_pk_fma_f32 v[76:77], v[186:187], v[68:69], v[184:185] op_sel_hi:[1,0,0]
	v_pk_fma_f32 v[68:69], v[84:85], v[68:69], v[184:185] op_sel_hi:[1,0,0]
	s_nop 0
	v_pk_fma_f32 v[68:69], v[82:83], v[66:67], v[68:69] op_sel_hi:[1,0,1]
	v_pk_fma_f32 v[66:67], v[74:75], v[66:67], v[76:77] op_sel_hi:[1,0,1]
	ds_read_b128 v[74:77], v123 offset:128
	ds_read_b128 v[82:85], v123 offset:192
	ds_read_b128 v[184:187], v112 offset:64
	ds_read_b128 v[188:191], v112 offset:4672
	ds_read_b128 v[192:195], v112 offset:9280
	ds_read_b128 v[196:199], v112 offset:13888
	ds_read_b128 v[200:203], v112 offset:18496
	ds_read_b128 v[204:207], v112 offset:23104
	ds_read_b128 v[208:211], v112 offset:27712
	ds_read_b128 v[212:215], v112 offset:32320
	s_waitcnt lgkmcnt(14)
	v_cvt_pk_bf16_f32 v62, v62, v63
	v_cvt_pk_bf16_f32 v63, v64, v65
	v_cvt_pk_bf16_f32 v64, v86, v87
	v_cvt_pk_bf16_f32 v65, v88, v89
	s_nop 1
	v_mfma_f32_16x16x32_bf16 v[86:89], v[90:93], v[62:65], v[164:167]
	v_mfma_f32_16x16x32_bf16 v[90:93], v[136:139], v[62:65], v[168:171]
	v_mfma_f32_16x16x32_bf16 v[136:139], v[140:143], v[62:65], v[172:175]
	v_mfma_f32_16x16x32_bf16 v[70:73], v[144:147], v[62:65], v[70:73]
	s_waitcnt lgkmcnt(13)
	v_mfma_f32_16x16x32_bf16 v[78:81], v[148:151], v[62:65], v[78:81]
	s_waitcnt lgkmcnt(12)
	v_mfma_f32_16x16x32_bf16 v[140:143], v[152:155], v[62:65], v[176:179]
	s_waitcnt lgkmcnt(11)
	v_mfma_f32_16x16x32_bf16 v[144:147], v[156:159], v[62:65], v[180:183]
	s_waitcnt lgkmcnt(10)
	v_mfma_f32_16x16x32_bf16 v[62:65], v[160:163], v[62:65], v[66:69]
	s_nop 2
	ds_read_b128 v[66:69], v123 offset:256
	ds_read_b128 v[148:151], v123 offset:320
	ds_read_b128 v[152:155], v112 offset:128
	ds_read_b128 v[156:159], v112 offset:4736
	ds_read_b128 v[160:163], v112 offset:9344
	ds_read_b128 v[164:167], v112 offset:13952
	ds_read_b128 v[168:171], v112 offset:18560
	ds_read_b128 v[172:175], v112 offset:23168
	ds_read_b128 v[176:179], v112 offset:27776
	ds_read_b128 v[180:183], v112 offset:32384
	s_waitcnt lgkmcnt(14)
	v_cvt_pk_bf16_f32 v74, v74, v75
	v_cvt_pk_bf16_f32 v75, v76, v77
	v_cvt_pk_bf16_f32 v76, v82, v83
	v_cvt_pk_bf16_f32 v77, v84, v85
	s_waitcnt lgkmcnt(10)
	s_nop 0
	v_mfma_f32_16x16x32_bf16 v[62:65], v[212:215], v[74:77], v[62:65]
	v_mfma_f32_16x16x32_bf16 v[82:85], v[184:187], v[74:77], v[86:89]
	v_mfma_f32_16x16x32_bf16 v[86:89], v[188:191], v[74:77], v[90:93]
	v_mfma_f32_16x16x32_bf16 v[90:93], v[192:195], v[74:77], v[136:139]
	v_mfma_f32_16x16x32_bf16 v[70:73], v[196:199], v[74:77], v[70:73]
	v_mfma_f32_16x16x32_bf16 v[78:81], v[200:203], v[74:77], v[78:81]
	v_mfma_f32_16x16x32_bf16 v[136:139], v[204:207], v[74:77], v[140:143]
	v_mfma_f32_16x16x32_bf16 v[140:143], v[208:211], v[74:77], v[144:147]
	ds_read_b128 v[74:77], v123 offset:384
	s_nop 1
	ds_read_b128 v[144:147], v123 offset:448
	ds_read_b128 v[184:187], v112 offset:192
	ds_read_b128 v[188:191], v112 offset:4800
	ds_read_b128 v[192:195], v112 offset:9408
	ds_read_b128 v[196:199], v112 offset:14016
	ds_read_b128 v[200:203], v112 offset:18624
	ds_read_b128 v[204:207], v112 offset:23232
	ds_read_b128 v[208:211], v112 offset:27840
	ds_read_b128 v[212:215], v112 offset:32448
	s_waitcnt lgkmcnt(14)
	v_cvt_pk_bf16_f32 v66, v66, v67
	v_cvt_pk_bf16_f32 v67, v68, v69
	v_cvt_pk_bf16_f32 v68, v148, v149
	v_cvt_pk_bf16_f32 v69, v150, v151
	s_waitcnt lgkmcnt(10)
	s_nop 0
	v_mfma_f32_16x16x32_bf16 v[62:65], v[180:183], v[66:69], v[62:65]
	v_mfma_f32_16x16x32_bf16 v[82:85], v[152:155], v[66:69], v[82:85]
	v_mfma_f32_16x16x32_bf16 v[86:89], v[156:159], v[66:69], v[86:89]
	v_mfma_f32_16x16x32_bf16 v[90:93], v[160:163], v[66:69], v[90:93]
	v_mfma_f32_16x16x32_bf16 v[70:73], v[164:167], v[66:69], v[70:73]
	v_mfma_f32_16x16x32_bf16 v[78:81], v[168:171], v[66:69], v[78:81]
	v_mfma_f32_16x16x32_bf16 v[136:139], v[172:175], v[66:69], v[136:139]
	v_mfma_f32_16x16x32_bf16 v[140:143], v[176:179], v[66:69], v[140:143]
	ds_read2st64_b64 v[66:69], v134 offset0:54 offset1:63
	ds_read2st64_b64 v[148:151], v134 offset0:36 offset1:45
	ds_read2st64_b64 v[152:155], v134 offset0:18 offset1:27
	ds_read2st64_b64 v[156:159], v134 offset1:9
	ds_read_b128 v[160:163], v124 offset:8704
	s_waitcnt lgkmcnt(14)
	v_cvt_pk_bf16_f32 v74, v74, v75
	v_cvt_pk_bf16_f32 v75, v76, v77
	s_waitcnt lgkmcnt(13)
	v_cvt_pk_bf16_f32 v76, v144, v145
	v_cvt_pk_bf16_f32 v77, v146, v147
	s_waitcnt lgkmcnt(5)
	s_nop 0
	v_mfma_f32_16x16x32_bf16 v[62:65], v[212:215], v[74:77], v[62:65]
	v_mfma_f32_16x16x32_bf16 v[82:85], v[184:187], v[74:77], v[82:85]
	v_mfma_f32_16x16x32_bf16 v[86:89], v[188:191], v[74:77], v[86:89]
	v_mfma_f32_16x16x32_bf16 v[90:93], v[192:195], v[74:77], v[90:93]
	v_mfma_f32_16x16x32_bf16 v[70:73], v[196:199], v[74:77], v[70:73]
	v_mfma_f32_16x16x32_bf16 v[78:81], v[200:203], v[74:77], v[78:81]
	v_mfma_f32_16x16x32_bf16 v[136:139], v[204:207], v[74:77], v[136:139]
	v_mfma_f32_16x16x32_bf16 v[140:143], v[208:211], v[74:77], v[140:143]
	ds_read_b128 v[144:147], v125
	ds_read_b128 v[164:167], v126
	ds_read_b128 v[168:171], v127
	ds_read_b128 v[172:175], v128
	ds_read_b128 v[176:179], v129
	ds_read_b128 v[180:183], v130
	ds_read_b128 v[184:187], v131
	ds_read_b128 v[188:191], v132
	ds_read_b128 v[192:195], v112 offset:36864
	ds_read_b128 v[196:199], v112 offset:41472
	ds_read_b128 v[200:203], v112 offset:46080
	ds_read_b128 v[204:207], v112 offset:50688
	ds_read_b128 v[208:211], v112 offset:55296
	ds_read_b128 v[212:215], v112 offset:59904
	ds_read_b128 v[216:219], v112 offset:64512
	ds_read_b128 v[220:223], v113 offset:32256
	s_waitcnt lgkmcnt(14)
	v_cvt_pk_bf16_f32 v74, v160, v161
	v_cvt_pk_bf16_f32 v75, v162, v163
	s_nop 1
	v_mfma_f32_16x16x16_bf16 v[160:163], v[156:157], v[74:75], v[82:85]
	v_mfma_f32_16x16x16_bf16 v[86:89], v[158:159], v[74:75], v[86:89]
	v_mfma_f32_16x16x16_bf16 v[90:93], v[152:153], v[74:75], v[90:93]
	v_mfma_f32_16x16x16_bf16 v[70:73], v[154:155], v[74:75], v[70:73]
	v_mfma_f32_16x16x16_bf16 v[78:81], v[148:149], v[74:75], v[78:81]
	v_mfma_f32_16x16x16_bf16 v[136:139], v[150:151], v[74:75], v[136:139]
	v_mfma_f32_16x16x16_bf16 v[82:85], v[66:67], v[74:75], v[140:143]
	v_mfma_f32_16x16x16_bf16 v[74:77], v[68:69], v[74:75], v[62:65]
	s_nop 2
	v_exp_f32_e32 v62, v160
	v_exp_f32_e32 v63, v161
	v_exp_f32_e32 v64, v162
	v_exp_f32_e32 v65, v163
	v_add_f32_e32 v62, 1.0, v62
	v_add_f32_e32 v63, 1.0, v63
	v_rcp_f32_e32 v62, v62
	v_rcp_f32_e32 v63, v63
	v_add_f32_e32 v64, 1.0, v64
	v_add_f32_e32 v65, 1.0, v65
	v_rcp_f32_e32 v64, v64
	v_rcp_f32_e32 v65, v65
	v_pk_mul_f32 v[62:63], v[160:161], v[62:63]
	v_exp_f32_e32 v66, v86
	v_cvt_pk_bf16_f32 v140, v62, v63
	v_pk_mul_f32 v[62:63], v[162:163], v[64:65]
	v_exp_f32_e32 v64, v88
	v_cvt_pk_bf16_f32 v141, v62, v63
	v_exp_f32_e32 v63, v87
	v_exp_f32_e32 v65, v89
	v_add_f32_e32 v62, 1.0, v66
	v_rcp_f32_e32 v62, v62
	v_add_f32_e32 v63, 1.0, v63
	v_rcp_f32_e32 v63, v63
	v_add_f32_e32 v64, 1.0, v64
	v_add_f32_e32 v65, 1.0, v65
	v_rcp_f32_e32 v64, v64
	v_rcp_f32_e32 v65, v65
	v_pk_mul_f32 v[62:63], v[86:87], v[62:63]
	v_exp_f32_e32 v66, v90
	v_cvt_pk_bf16_f32 v142, v62, v63
	v_pk_mul_f32 v[62:63], v[88:89], v[64:65]
	v_exp_f32_e32 v64, v92
	v_cvt_pk_bf16_f32 v143, v62, v63
	v_exp_f32_e32 v63, v91
	v_exp_f32_e32 v65, v93
	v_add_f32_e32 v62, 1.0, v66
	v_rcp_f32_e32 v62, v62
	v_add_f32_e32 v63, 1.0, v63
	v_rcp_f32_e32 v63, v63
	v_add_f32_e32 v64, 1.0, v64
	v_add_f32_e32 v65, 1.0, v65
	v_rcp_f32_e32 v64, v64
	v_rcp_f32_e32 v65, v65
	v_pk_mul_f32 v[62:63], v[90:91], v[62:63]
	v_exp_f32_e32 v66, v70
	v_cvt_pk_bf16_f32 v86, v62, v63
	v_pk_mul_f32 v[62:63], v[92:93], v[64:65]
	v_exp_f32_e32 v64, v72
	v_cvt_pk_bf16_f32 v87, v62, v63
	v_exp_f32_e32 v63, v71
	v_exp_f32_e32 v65, v73
	v_add_f32_e32 v62, 1.0, v66
	v_rcp_f32_e32 v62, v62
	v_add_f32_e32 v63, 1.0, v63
	v_rcp_f32_e32 v63, v63
	v_add_f32_e32 v64, 1.0, v64
	v_add_f32_e32 v65, 1.0, v65
	v_rcp_f32_e32 v64, v64
	v_rcp_f32_e32 v65, v65
	v_pk_mul_f32 v[62:63], v[70:71], v[62:63]
	v_exp_f32_e32 v66, v78
	v_cvt_pk_bf16_f32 v88, v62, v63
	v_pk_mul_f32 v[62:63], v[72:73], v[64:65]
	v_exp_f32_e32 v64, v80
	v_cvt_pk_bf16_f32 v89, v62, v63
	v_exp_f32_e32 v63, v79
	v_exp_f32_e32 v65, v81
	v_add_f32_e32 v62, 1.0, v66
	v_rcp_f32_e32 v62, v62
	v_add_f32_e32 v63, 1.0, v63
	v_rcp_f32_e32 v63, v63
	v_add_f32_e32 v64, 1.0, v64
	v_add_f32_e32 v65, 1.0, v65
	v_rcp_f32_e32 v64, v64
	v_rcp_f32_e32 v65, v65
	v_exp_f32_e32 v66, v136
	v_pk_mul_f32 v[62:63], v[78:79], v[62:63]
	v_exp_f32_e32 v67, v139
	v_cvt_pk_bf16_f32 v148, v62, v63
	v_pk_mul_f32 v[62:63], v[80:81], v[64:65]
	v_exp_f32_e32 v65, v137
	v_add_f32_e32 v64, 1.0, v66
	v_exp_f32_e32 v66, v138
	v_rcp_f32_e32 v64, v64
	v_add_f32_e32 v65, 1.0, v65
	v_rcp_f32_e32 v65, v65
	v_add_f32_e32 v66, 1.0, v66
	v_add_f32_e32 v67, 1.0, v67
	v_rcp_f32_e32 v66, v66
	v_rcp_f32_e32 v67, v67
	v_cvt_pk_bf16_f32 v149, v62, v63
	v_pk_mul_f32 v[62:63], v[136:137], v[64:65]
	s_nop 0
	v_cvt_pk_bf16_f32 v150, v62, v63
	v_pk_mul_f32 v[62:63], v[138:139], v[66:67]
	s_nop 0
	v_cvt_pk_bf16_f32 v151, v62, v63
	ds_read_b128 v[90:93], v112 offset:36928
	ds_read_b128 v[136:139], v112 offset:41536
	ds_read_b128 v[152:155], v112 offset:46144
	ds_read_b128 v[156:159], v112 offset:50752
	ds_read_b128 v[160:163], v112 offset:55360
	ds_read_b128 v[224:227], v112 offset:59968
	ds_read_b128 v[228:231], v112 offset:64576
	ds_read_b128 v[232:235], v113 offset:32320
	ds_read_b128 v[62:65], v123
	ds_read_b128 v[66:69], v123 offset:64
	s_waitcnt lgkmcnt(14)
	v_mfma_f32_16x16x32_bf16 v[144:147], v[192:195], v[140:143], v[144:147]
	v_mfma_f32_16x16x32_bf16 v[164:167], v[196:199], v[140:143], v[164:167]
	v_mfma_f32_16x16x32_bf16 v[168:171], v[200:203], v[140:143], v[168:171]
	v_mfma_f32_16x16x32_bf16 v[172:175], v[204:207], v[140:143], v[172:175]
	s_waitcnt lgkmcnt(13)
	v_mfma_f32_16x16x32_bf16 v[176:179], v[208:211], v[140:143], v[176:179]
	s_waitcnt lgkmcnt(12)
	v_mfma_f32_16x16x32_bf16 v[180:183], v[212:215], v[140:143], v[180:183]
	s_waitcnt lgkmcnt(11)
	v_mfma_f32_16x16x32_bf16 v[184:187], v[216:219], v[140:143], v[184:187]
	s_waitcnt lgkmcnt(10)
	v_mfma_f32_16x16x32_bf16 v[140:143], v[220:223], v[140:143], v[188:191]
	s_nop 2
	ds_read_b128 v[188:191], v112 offset:36992
	ds_read_b128 v[192:195], v112 offset:41600
	ds_read_b128 v[196:199], v112 offset:46208
	ds_read_b128 v[200:203], v112 offset:50816
	ds_read_b128 v[204:207], v112 offset:55424
	ds_read_b128 v[208:211], v112 offset:60032
	ds_read_b128 v[212:215], v112 offset:64640
	ds_read_b128 v[216:219], v113 offset:32384
	ds_read_b128 v[70:73], v123 offset:128
	ds_read_b128 v[78:81], v123 offset:192
	s_waitcnt lgkmcnt(14)
	v_mfma_f32_16x16x32_bf16 v[144:147], v[90:93], v[86:89], v[144:147]
	v_mfma_f32_16x16x32_bf16 v[136:139], v[136:139], v[86:89], v[164:167]
	v_mfma_f32_16x16x32_bf16 v[152:155], v[152:155], v[86:89], v[168:171]
	v_mfma_f32_16x16x32_bf16 v[156:159], v[156:159], v[86:89], v[172:175]
	v_mfma_f32_16x16x32_bf16 v[160:163], v[160:163], v[86:89], v[176:179]
	v_mfma_f32_16x16x32_bf16 v[164:167], v[224:227], v[86:89], v[180:183]
	s_waitcnt lgkmcnt(13)
	v_mfma_f32_16x16x32_bf16 v[168:171], v[228:231], v[86:89], v[184:187]
	s_waitcnt lgkmcnt(12)
	v_mfma_f32_16x16x32_bf16 v[140:143], v[232:235], v[86:89], v[140:143]
	ds_read_b128 v[172:175], v112 offset:37056
	ds_read_b128 v[176:179], v112 offset:41664
	ds_read_b128 v[180:183], v112 offset:46272
	ds_read_b128 v[184:187], v112 offset:50880
	ds_read_b128 v[220:223], v112 offset:55488
	ds_read_b128 v[224:227], v112 offset:60096
	ds_read_b128 v[228:231], v112 offset:64704
	ds_read_b128 v[232:235], v113 offset:32448
	ds_read_b128 v[86:89], v123 offset:256
	ds_read_b128 v[90:93], v123 offset:320
	s_waitcnt lgkmcnt(14)
	v_mfma_f32_16x16x32_bf16 v[144:147], v[188:191], v[148:151], v[144:147]
	v_mfma_f32_16x16x32_bf16 v[136:139], v[192:195], v[148:151], v[136:139]
	v_mfma_f32_16x16x32_bf16 v[152:155], v[196:199], v[148:151], v[152:155]
	v_mfma_f32_16x16x32_bf16 v[156:159], v[200:203], v[148:151], v[156:159]
	v_mfma_f32_16x16x32_bf16 v[160:163], v[204:207], v[148:151], v[160:163]
	v_mfma_f32_16x16x32_bf16 v[164:167], v[208:211], v[148:151], v[164:167]
	s_waitcnt lgkmcnt(13)
	v_mfma_f32_16x16x32_bf16 v[168:171], v[212:215], v[148:151], v[168:171]
	s_waitcnt lgkmcnt(12)
	v_mfma_f32_16x16x32_bf16 v[140:143], v[216:219], v[148:151], v[140:143]
	v_exp_f32_e32 v148, v82
	v_exp_f32_e32 v149, v83
	v_exp_f32_e32 v150, v84
	v_exp_f32_e32 v151, v85
	v_add_f32_e32 v148, 1.0, v148
	v_add_f32_e32 v149, 1.0, v149
	v_rcp_f32_e32 v148, v148
	v_rcp_f32_e32 v149, v149
	v_add_f32_e32 v150, 1.0, v150
	v_add_f32_e32 v151, 1.0, v151
	v_rcp_f32_e32 v150, v150
	v_rcp_f32_e32 v151, v151
	v_pk_mul_f32 v[82:83], v[82:83], v[148:149]
	v_exp_f32_e32 v148, v74
	v_cvt_pk_bf16_f32 v82, v82, v83
	v_pk_mul_f32 v[84:85], v[84:85], v[150:151]
	v_exp_f32_e32 v149, v77
	v_cvt_pk_bf16_f32 v83, v84, v85
	v_exp_f32_e32 v85, v75
	v_add_f32_e32 v84, 1.0, v148
	v_exp_f32_e32 v148, v76
	v_rcp_f32_e32 v84, v84
	v_add_f32_e32 v85, 1.0, v85
	v_rcp_f32_e32 v85, v85
	v_add_f32_e32 v148, 1.0, v148
	v_rcp_f32_e32 v192, v148
	v_add_f32_e32 v148, 1.0, v149
	v_rcp_f32_e32 v193, v148
	ds_read_b128 v[148:151], v123 offset:384
	ds_read_b128 v[188:191], v123 offset:448
	v_pk_mul_f32 v[74:75], v[74:75], v[84:85]
	s_nop 0
	v_cvt_pk_bf16_f32 v84, v74, v75
	v_pk_mul_f32 v[74:75], v[76:77], v[192:193]
	s_nop 0
	v_cvt_pk_bf16_f32 v85, v74, v75
	s_waitcnt lgkmcnt(11)
	s_nop 0
	v_mfma_f32_16x16x32_bf16 v[74:77], v[172:175], v[82:85], v[144:147]
	s_waitcnt lgkmcnt(10)
	v_mfma_f32_16x16x32_bf16 v[136:139], v[176:179], v[82:85], v[136:139]
	s_waitcnt lgkmcnt(9)
	v_mfma_f32_16x16x32_bf16 v[144:147], v[180:183], v[82:85], v[152:155]
	s_waitcnt lgkmcnt(8)
	v_mfma_f32_16x16x32_bf16 v[152:155], v[184:187], v[82:85], v[156:159]
	s_waitcnt lgkmcnt(7)
	v_mfma_f32_16x16x32_bf16 v[156:159], v[220:223], v[82:85], v[160:163]
	s_waitcnt lgkmcnt(6)
	v_mfma_f32_16x16x32_bf16 v[160:163], v[224:227], v[82:85], v[164:167]
	s_waitcnt lgkmcnt(5)
	v_mfma_f32_16x16x32_bf16 v[164:167], v[228:231], v[82:85], v[168:171]
	s_waitcnt lgkmcnt(4)
	v_mfma_f32_16x16x32_bf16 v[82:85], v[232:235], v[82:85], v[140:143]
	s_nop 2
	v_exp_f32_e32 v140, v74
	v_exp_f32_e32 v141, v75
	v_exp_f32_e32 v168, v136
	v_exp_f32_e32 v169, v137
	v_exp_f32_e32 v170, v138
	v_exp_f32_e32 v171, v139
	v_exp_f32_e32 v142, v76
	v_exp_f32_e32 v143, v77
	v_add_f32_e32 v140, 1.0, v140
	v_add_f32_e32 v141, 1.0, v141
	v_rcp_f32_e32 v140, v140
	v_rcp_f32_e32 v141, v141
	v_add_f32_e32 v168, 1.0, v168
	v_add_f32_e32 v169, 1.0, v169
	v_rcp_f32_e32 v168, v168
	v_rcp_f32_e32 v169, v169
	v_add_f32_e32 v170, 1.0, v170
	v_add_f32_e32 v171, 1.0, v171
	v_add_f32_e32 v142, 1.0, v142
	v_add_f32_e32 v143, 1.0, v143
	v_rcp_f32_e32 v170, v170
	v_rcp_f32_e32 v171, v171
	v_rcp_f32_e32 v142, v142
	v_rcp_f32_e32 v143, v143
	v_exp_f32_e32 v172, v144
	v_exp_f32_e32 v173, v145
	v_pk_mul_f32 v[74:75], v[74:75], v[140:141]
	v_pk_mul_f32 v[136:137], v[136:137], v[168:169]
	v_pk_fma_f32 v[62:63], v[74:75], s[2:3], v[62:63] op_sel_hi:[1,0,1]
	v_exp_f32_e32 v174, v146
	v_exp_f32_e32 v175, v147
	v_pk_fma_f32 v[66:67], v[136:137], s[2:3], v[66:67] op_sel_hi:[1,0,1]
	v_pk_mul_f32 v[136:137], v[138:139], v[170:171]
	v_add_f32_e32 v74, 0, v62
	v_pk_fma_f32 v[68:69], v[136:137], s[2:3], v[68:69] op_sel_hi:[1,0,1]
	v_add_f32_e32 v136, v63, v74
	v_pk_mul_f32 v[74:75], v[76:77], v[142:143]
	v_add_f32_e32 v172, 1.0, v172
	v_add_f32_e32 v173, 1.0, v173
	v_exp_f32_e32 v176, v152
	v_exp_f32_e32 v177, v153
	v_pk_fma_f32 v[64:65], v[74:75], s[2:3], v[64:65] op_sel_hi:[1,0,1]
	v_rcp_f32_e32 v172, v172
	v_rcp_f32_e32 v173, v173
	v_add_f32_e32 v74, v64, v136
	v_add_f32_e32 v174, 1.0, v174
	v_add_f32_e32 v175, 1.0, v175
	v_exp_f32_e32 v178, v154
	v_exp_f32_e32 v179, v155
	v_add_f32_e32 v74, v65, v74
	v_rcp_f32_e32 v174, v174
	v_rcp_f32_e32 v175, v175
	v_add_f32_e32 v74, v66, v74
	v_add_f32_e32 v176, 1.0, v176
	v_add_f32_e32 v177, 1.0, v177
	v_exp_f32_e32 v180, v156
	v_exp_f32_e32 v181, v157
	v_add_f32_e32 v74, v67, v74
	v_rcp_f32_e32 v176, v176
	v_rcp_f32_e32 v177, v177
	v_pk_mul_f32 v[144:145], v[144:145], v[172:173]
	v_add_f32_e32 v74, v68, v74
	v_add_f32_e32 v178, 1.0, v178
	v_add_f32_e32 v179, 1.0, v179
	v_exp_f32_e32 v182, v158
	v_exp_f32_e32 v183, v159
	v_pk_fma_f32 v[70:71], v[144:145], s[2:3], v[70:71] op_sel_hi:[1,0,1]
	v_add_f32_e32 v74, v69, v74
	v_rcp_f32_e32 v178, v178
	v_rcp_f32_e32 v179, v179
	v_pk_mul_f32 v[144:145], v[146:147], v[174:175]
	v_add_f32_e32 v74, v70, v74
	v_add_f32_e32 v180, 1.0, v180
	v_add_f32_e32 v181, 1.0, v181
	v_exp_f32_e32 v184, v160
	v_exp_f32_e32 v185, v161
	v_pk_fma_f32 v[72:73], v[144:145], s[2:3], v[72:73] op_sel_hi:[1,0,1]
	v_add_f32_e32 v74, v71, v74
	v_rcp_f32_e32 v180, v180
	v_rcp_f32_e32 v181, v181
	v_pk_mul_f32 v[152:153], v[152:153], v[176:177]
	v_add_f32_e32 v74, v72, v74
	v_add_f32_e32 v182, 1.0, v182
	v_add_f32_e32 v183, 1.0, v183
	v_exp_f32_e32 v186, v162
	v_exp_f32_e32 v187, v163
	v_pk_fma_f32 v[78:79], v[152:153], s[2:3], v[78:79] op_sel_hi:[1,0,1]
	v_add_f32_e32 v74, v73, v74
	v_rcp_f32_e32 v182, v182
	v_rcp_f32_e32 v183, v183
	v_pk_mul_f32 v[152:153], v[154:155], v[178:179]
	v_add_f32_e32 v74, v78, v74
	v_add_f32_e32 v184, 1.0, v184
	v_add_f32_e32 v185, 1.0, v185
	v_exp_f32_e32 v192, v164
	v_exp_f32_e32 v193, v165
	v_pk_fma_f32 v[80:81], v[152:153], s[2:3], v[80:81] op_sel_hi:[1,0,1]
	v_add_f32_e32 v74, v79, v74
	v_rcp_f32_e32 v184, v184
	v_rcp_f32_e32 v185, v185
	v_pk_mul_f32 v[156:157], v[156:157], v[180:181]
	v_add_f32_e32 v74, v80, v74
	v_add_f32_e32 v186, 1.0, v186
	v_add_f32_e32 v187, 1.0, v187
	v_exp_f32_e32 v194, v166
	v_exp_f32_e32 v195, v167
	s_waitcnt lgkmcnt(3)
	v_pk_fma_f32 v[86:87], v[156:157], s[2:3], v[86:87] op_sel_hi:[1,0,1]
	v_add_f32_e32 v74, v81, v74
	v_rcp_f32_e32 v186, v186
	v_rcp_f32_e32 v187, v187
	v_pk_mul_f32 v[156:157], v[158:159], v[182:183]
	v_add_f32_e32 v74, v86, v74
	v_add_f32_e32 v192, 1.0, v192
	v_add_f32_e32 v193, 1.0, v193
	v_exp_f32_e32 v196, v82
	v_exp_f32_e32 v197, v83
	v_pk_fma_f32 v[88:89], v[156:157], s[2:3], v[88:89] op_sel_hi:[1,0,1]
	v_add_f32_e32 v74, v87, v74
	v_rcp_f32_e32 v192, v192
	v_rcp_f32_e32 v193, v193
	v_pk_mul_f32 v[160:161], v[160:161], v[184:185]
	v_add_f32_e32 v74, v88, v74
	v_add_f32_e32 v194, 1.0, v194
	v_add_f32_e32 v195, 1.0, v195
	v_exp_f32_e32 v198, v84
	v_exp_f32_e32 v199, v85
	s_waitcnt lgkmcnt(2)
	v_pk_fma_f32 v[90:91], v[160:161], s[2:3], v[90:91] op_sel_hi:[1,0,1]
	v_add_f32_e32 v74, v89, v74
	v_rcp_f32_e32 v194, v194
	v_rcp_f32_e32 v195, v195
	v_pk_mul_f32 v[160:161], v[162:163], v[186:187]
	v_add_f32_e32 v74, v90, v74
	v_add_f32_e32 v196, 1.0, v196
	v_add_f32_e32 v197, 1.0, v197
	v_pk_fma_f32 v[92:93], v[160:161], s[2:3], v[92:93] op_sel_hi:[1,0,1]
	v_add_f32_e32 v74, v91, v74
	v_rcp_f32_e32 v196, v196
	v_rcp_f32_e32 v197, v197
	v_pk_mul_f32 v[164:165], v[164:165], v[192:193]
	v_add_f32_e32 v74, v92, v74
	v_add_f32_e32 v198, 1.0, v198
	v_add_f32_e32 v199, 1.0, v199
	s_waitcnt lgkmcnt(1)
	v_pk_fma_f32 v[148:149], v[164:165], s[2:3], v[148:149] op_sel_hi:[1,0,1]
	v_add_f32_e32 v74, v93, v74
	v_rcp_f32_e32 v198, v198
	v_rcp_f32_e32 v199, v199
	v_pk_mul_f32 v[164:165], v[166:167], v[194:195]
	v_add_f32_e32 v74, v148, v74
	v_pk_fma_f32 v[150:151], v[164:165], s[2:3], v[150:151] op_sel_hi:[1,0,1]
	v_add_f32_e32 v74, v149, v74
	v_pk_mul_f32 v[82:83], v[82:83], v[196:197]
	v_add_f32_e32 v74, v150, v74
	s_waitcnt lgkmcnt(0)
	v_pk_fma_f32 v[82:83], v[82:83], s[2:3], v[188:189] op_sel_hi:[1,0,1]
	v_add_f32_e32 v74, v151, v74
	v_pk_mul_f32 v[84:85], v[84:85], v[198:199]
	v_add_f32_e32 v74, v82, v74
	v_pk_fma_f32 v[84:85], v[84:85], s[2:3], v[190:191] op_sel_hi:[1,0,1]
	v_add_f32_e32 v74, v83, v74
	v_add_f32_e32 v74, v84, v74
	v_add_f32_e32 v74, v85, v74
	ds_bpermute_b32 v75, v116, v74
	s_waitcnt lgkmcnt(0)
	v_add_f32_e32 v74, v74, v75
	ds_bpermute_b32 v75, v117, v74
	s_waitcnt lgkmcnt(0)
	v_add_f32_e32 v74, v74, v75
	v_mul_f32_e32 v74, 0x3c000000, v74
	v_pk_add_f32 v[62:63], v[62:63], v[74:75] op_sel_hi:[1,0] neg_lo:[0,1] neg_hi:[0,1]
	v_pk_add_f32 v[64:65], v[64:65], v[74:75] op_sel_hi:[1,0] neg_lo:[0,1] neg_hi:[0,1]
	v_pk_mul_f32 v[76:77], v[62:63], v[62:63]
	v_pk_mul_f32 v[136:137], v[64:65], v[64:65]
	v_add_f32_e32 v76, v76, v77
	v_pk_add_f32 v[66:67], v[66:67], v[74:75] op_sel_hi:[1,0] neg_lo:[0,1] neg_hi:[0,1]
	v_add_f32_e32 v76, v136, v76
	v_pk_mul_f32 v[138:139], v[66:67], v[66:67]
	v_add_f32_e32 v76, v137, v76
	v_pk_add_f32 v[68:69], v[68:69], v[74:75] op_sel_hi:[1,0] neg_lo:[0,1] neg_hi:[0,1]
	v_add_f32_e32 v76, v138, v76
	v_pk_mul_f32 v[140:141], v[68:69], v[68:69]
	v_add_f32_e32 v76, v139, v76
	v_pk_add_f32 v[70:71], v[70:71], v[74:75] op_sel_hi:[1,0] neg_lo:[0,1] neg_hi:[0,1]
	v_add_f32_e32 v76, v140, v76
	v_pk_mul_f32 v[142:143], v[70:71], v[70:71]
	v_add_f32_e32 v76, v141, v76
	v_pk_add_f32 v[72:73], v[72:73], v[74:75] op_sel_hi:[1,0] neg_lo:[0,1] neg_hi:[0,1]
	v_add_f32_e32 v76, v142, v76
	v_pk_mul_f32 v[144:145], v[72:73], v[72:73]
	v_add_f32_e32 v76, v143, v76
	v_pk_add_f32 v[78:79], v[78:79], v[74:75] op_sel_hi:[1,0] neg_lo:[0,1] neg_hi:[0,1]
	v_add_f32_e32 v76, v144, v76
	v_pk_mul_f32 v[146:147], v[78:79], v[78:79]
	v_add_f32_e32 v76, v145, v76
	v_pk_add_f32 v[80:81], v[80:81], v[74:75] op_sel_hi:[1,0] neg_lo:[0,1] neg_hi:[0,1]
	v_add_f32_e32 v76, v146, v76
	v_pk_mul_f32 v[152:153], v[80:81], v[80:81]
	v_add_f32_e32 v76, v147, v76
	v_pk_add_f32 v[86:87], v[86:87], v[74:75] op_sel_hi:[1,0] neg_lo:[0,1] neg_hi:[0,1]
	v_add_f32_e32 v76, v152, v76
	v_pk_mul_f32 v[154:155], v[86:87], v[86:87]
	v_add_f32_e32 v76, v153, v76
	v_pk_add_f32 v[88:89], v[88:89], v[74:75] op_sel_hi:[1,0] neg_lo:[0,1] neg_hi:[0,1]
	v_add_f32_e32 v76, v154, v76
	v_pk_mul_f32 v[156:157], v[88:89], v[88:89]
	v_add_f32_e32 v76, v155, v76
	v_pk_add_f32 v[90:91], v[90:91], v[74:75] op_sel_hi:[1,0] neg_lo:[0,1] neg_hi:[0,1]
	v_add_f32_e32 v76, v156, v76
	v_pk_mul_f32 v[158:159], v[90:91], v[90:91]
	v_add_f32_e32 v76, v157, v76
	v_pk_add_f32 v[92:93], v[92:93], v[74:75] op_sel_hi:[1,0] neg_lo:[0,1] neg_hi:[0,1]
	v_add_f32_e32 v76, v158, v76
	v_pk_mul_f32 v[160:161], v[92:93], v[92:93]
	v_add_f32_e32 v76, v159, v76
	v_pk_add_f32 v[148:149], v[148:149], v[74:75] op_sel_hi:[1,0] neg_lo:[0,1] neg_hi:[0,1]
	v_add_f32_e32 v76, v160, v76
	v_pk_mul_f32 v[162:163], v[148:149], v[148:149]
	v_add_f32_e32 v76, v161, v76
	v_pk_add_f32 v[150:151], v[150:151], v[74:75] op_sel_hi:[1,0] neg_lo:[0,1] neg_hi:[0,1]
	v_add_f32_e32 v76, v162, v76
	v_pk_mul_f32 v[164:165], v[150:151], v[150:151]
	v_add_f32_e32 v76, v163, v76
	v_pk_add_f32 v[82:83], v[82:83], v[74:75] op_sel_hi:[1,0] neg_lo:[0,1] neg_hi:[0,1]
	v_add_f32_e32 v76, v164, v76
	v_pk_mul_f32 v[166:167], v[82:83], v[82:83]
	v_add_f32_e32 v76, v165, v76
	v_pk_add_f32 v[74:75], v[84:85], v[74:75] op_sel_hi:[1,0] neg_lo:[0,1] neg_hi:[0,1]
	v_add_f32_e32 v76, v166, v76
	v_pk_mul_f32 v[84:85], v[74:75], v[74:75]
	v_add_f32_e32 v76, v167, v76
	v_add_f32_e32 v76, v84, v76
	v_add_f32_e32 v76, v85, v76
	ds_bpermute_b32 v77, v116, v76
	s_waitcnt lgkmcnt(0)
	v_add_f32_e32 v76, v76, v77
	ds_bpermute_b32 v77, v117, v76
	s_waitcnt lgkmcnt(0)
	v_add_f32_e32 v76, v76, v77
	v_fmamk_f32 v76, v76, 0x3c000000, v133
	v_rsq_f32_e32 v76, v76
	s_nop 0
	v_pk_mul_f32 v[64:65], v[64:65], v[76:77] op_sel_hi:[1,0]
	v_pk_mul_f32 v[62:63], v[62:63], v[76:77] op_sel_hi:[1,0]
	ds_write_b128 v123, v[62:65]
	v_pk_mul_f32 v[64:65], v[68:69], v[76:77] op_sel_hi:[1,0]
	v_pk_mul_f32 v[62:63], v[66:67], v[76:77] op_sel_hi:[1,0]
	ds_write_b128 v123, v[62:65] offset:64
	v_pk_mul_f32 v[64:65], v[72:73], v[76:77] op_sel_hi:[1,0]
	v_pk_mul_f32 v[62:63], v[70:71], v[76:77] op_sel_hi:[1,0]
	ds_write_b128 v123, v[62:65] offset:128
	v_pk_mul_f32 v[64:65], v[80:81], v[76:77] op_sel_hi:[1,0]
	v_pk_mul_f32 v[62:63], v[78:79], v[76:77] op_sel_hi:[1,0]
	ds_write_b128 v123, v[62:65] offset:192
	v_pk_mul_f32 v[64:65], v[88:89], v[76:77] op_sel_hi:[1,0]
	v_pk_mul_f32 v[62:63], v[86:87], v[76:77] op_sel_hi:[1,0]
	ds_write_b128 v123, v[62:65] offset:256
	v_pk_mul_f32 v[64:65], v[92:93], v[76:77] op_sel_hi:[1,0]
	v_pk_mul_f32 v[62:63], v[90:91], v[76:77] op_sel_hi:[1,0]
	ds_write_b128 v123, v[62:65] offset:320
	v_pk_mul_f32 v[64:65], v[150:151], v[76:77] op_sel_hi:[1,0]
	v_pk_mul_f32 v[62:63], v[148:149], v[76:77] op_sel_hi:[1,0]
	ds_write_b128 v123, v[62:65] offset:384
	v_pk_mul_f32 v[64:65], v[74:75], v[76:77] op_sel_hi:[1,0]
	v_pk_mul_f32 v[62:63], v[82:83], v[76:77] op_sel_hi:[1,0]
	ds_write_b128 v123, v[62:65] offset:448
	ds_read_b128 v[62:65], v121
	ds_read_b128 v[66:69], v121 offset:1088
	ds_read_b128 v[70:73], v121 offset:2176
	ds_read_b128 v[74:77], v121 offset:3264
	ds_read_b128 v[78:81], v121 offset:4352
	ds_read_b128 v[82:85], v121 offset:5440
	ds_read_b128 v[86:89], v121 offset:6528
	ds_read_b128 v[90:93], v121 offset:7616
	v_add_u32_e32 v136, 0xffffe400, v118
	s_waitcnt vmcnt(15) lgkmcnt(7)
	v_pk_fma_f32 v[64:65], v[56:57], v[64:65], v[60:61]
	v_pk_fma_f32 v[62:63], v[54:55], v[62:63], v[58:59]
	buffer_store_dwordx4 v[62:65], v136, s[4:7], 0 offen sc0 nt sc1
	v_cmp_lt_i32_e32 vcc, s8, v0
	s_or_b64 s[0:1], vcc, s[0:1]
	s_waitcnt lgkmcnt(6)
	v_pk_fma_f32 v[64:65], v[56:57], v[68:69], v[60:61]
	v_pk_fma_f32 v[62:63], v[54:55], v[66:67], v[58:59]
	v_add_u32_e32 v66, 0xffffe800, v118
	buffer_store_dwordx4 v[62:65], v66, s[4:7], 0 offen sc0 nt sc1
	v_add_u32_e32 v66, 0xffffec00, v118
	s_waitcnt lgkmcnt(5)
	v_pk_fma_f32 v[64:65], v[56:57], v[72:73], v[60:61]
	v_pk_fma_f32 v[62:63], v[54:55], v[70:71], v[58:59]
	buffer_store_dwordx4 v[62:65], v66, s[4:7], 0 offen sc0 nt sc1
	v_add_u32_e32 v66, 0xfffff000, v118
	s_waitcnt lgkmcnt(4)
	v_pk_fma_f32 v[64:65], v[56:57], v[76:77], v[60:61]
	v_pk_fma_f32 v[62:63], v[54:55], v[74:75], v[58:59]
	buffer_store_dwordx4 v[62:65], v66, s[4:7], 0 offen sc0 nt sc1
	v_add_u32_e32 v66, 0xfffff400, v118
	s_waitcnt lgkmcnt(3)
	v_pk_fma_f32 v[64:65], v[56:57], v[80:81], v[60:61]
	v_pk_fma_f32 v[62:63], v[54:55], v[78:79], v[58:59]
	buffer_store_dwordx4 v[62:65], v66, s[4:7], 0 offen sc0 nt sc1
	v_add_u32_e32 v66, 0xfffff800, v118
	s_waitcnt lgkmcnt(2)
	v_pk_fma_f32 v[64:65], v[56:57], v[84:85], v[60:61]
	v_pk_fma_f32 v[62:63], v[54:55], v[82:83], v[58:59]
	buffer_store_dwordx4 v[62:65], v66, s[4:7], 0 offen sc0 nt sc1
	v_add_u32_e32 v66, 0xfffffc00, v118
	s_waitcnt lgkmcnt(1)
	v_pk_fma_f32 v[64:65], v[56:57], v[88:89], v[60:61]
	v_pk_fma_f32 v[62:63], v[54:55], v[86:87], v[58:59]
	buffer_store_dwordx4 v[62:65], v66, s[4:7], 0 offen sc0 nt sc1
	s_waitcnt lgkmcnt(0)
	s_nop 0
	v_pk_fma_f32 v[64:65], v[56:57], v[92:93], v[60:61]
	v_pk_fma_f32 v[62:63], v[54:55], v[90:91], v[58:59]
	buffer_store_dwordx4 v[62:65], v118, s[4:7], 0 offen sc0 nt sc1
	v_add_u32_e32 v118, 0x1000000, v118
	s_nop 0
	v_mov_b32_e32 v62, v0
	s_waitcnt vmcnt(21)
	v_mov_b32_e32 v64, v135
	s_andn2_b64 exec, exec, s[0:1]
	s_cbranch_execnz .LBB1_6
